# speedup vs baseline: 1.0107x; 1.0017x over previous
.Lg1a_fin4:
	s_cmp_gt_i32 s61, 40
	s_cbranch_scc1 .Lg1a_fin1
	s_add_i32 s0, s33, s61
	s_cmpk_gt_u32 s0, 0x15ff
	s_cselect_b32 s2, 0x7fffea00, 0
	s_cselect_b32 s4, s25, s15
	s_cselect_b32 s5, s24, s14
	s_cselect_b32 s6, 0x80, 0
	s_add_i32 s0, s0, s2
	s_lshl_b32 s7, s0, 1
	s_add_i32 s0, s7, 0x2c00
	s_lshl_b64 s[2:3], s[0:1], 12
	s_mul_hi_u32 s8, s0, 0xba2e8ba3
	s_add_u32 s2, s5, s2
	s_addc_u32 s3, s4, s3
	s_lshr_b32 s4, s8, 11
	v_lshl_add_u64 v[6:7], s[2:3], 0, v[0:1]
	s_mul_i32 s2, s4, 0x7ffff500
	s_add_i32 s2, s2, s0
	s_mul_i32 s4, s4, 22
	s_lshr_b32 s0, s2, 7
	s_add_i32 s0, s0, s4
	s_lshl_b32 s0, s0, 8
	s_and_b32 s5, s7, 0x7e
	s_or_b32 s0, s0, s6
	global_load_dwordx4 v[8:11], v[6:7], off nt
	s_or_b32 s96, s0, s5
	s_add_i32 s0, s33, s61
	s_add_i32 s0, s0, 1
	s_cmpk_gt_u32 s0, 0x15ff
	s_cselect_b32 s2, 0x7fffea00, 0
	s_cselect_b32 s4, s25, s15
	s_cselect_b32 s5, s24, s14
	s_cselect_b32 s6, 0x80, 0
	s_add_i32 s0, s0, s2
	s_lshl_b32 s7, s0, 1
	s_add_i32 s0, s7, 0x2c00
	s_lshl_b64 s[2:3], s[0:1], 12
	s_mul_hi_u32 s8, s0, 0xba2e8ba3
	s_add_u32 s2, s5, s2
	s_addc_u32 s3, s4, s3
	s_lshr_b32 s4, s8, 11
	v_lshl_add_u64 v[6:7], s[2:3], 0, v[0:1]
	s_mul_i32 s2, s4, 0x7ffff500
	s_add_i32 s2, s2, s0
	s_mul_i32 s4, s4, 22
	s_lshr_b32 s0, s2, 7
	s_add_i32 s0, s0, s4
	s_lshl_b32 s0, s0, 8
	s_and_b32 s5, s7, 0x7e
	s_or_b32 s0, s0, s6
	global_load_dwordx4 v[12:15], v[6:7], off nt
	s_or_b32 s97, s0, s5
	s_add_i32 s0, s33, s61
	s_add_i32 s0, s0, 2
	s_cmpk_gt_u32 s0, 0x15ff
	s_cselect_b32 s2, 0x7fffea00, 0
	s_cselect_b32 s4, s25, s15
	s_cselect_b32 s5, s24, s14
	s_cselect_b32 s6, 0x80, 0
	s_add_i32 s0, s0, s2
	s_lshl_b32 s7, s0, 1
	s_add_i32 s0, s7, 0x2c00
	s_lshl_b64 s[2:3], s[0:1], 12
	s_mul_hi_u32 s8, s0, 0xba2e8ba3
	s_add_u32 s2, s5, s2
	s_addc_u32 s3, s4, s3
	s_lshr_b32 s4, s8, 11
	v_lshl_add_u64 v[6:7], s[2:3], 0, v[0:1]
	s_mul_i32 s2, s4, 0x7ffff500
	s_add_i32 s2, s2, s0
	s_mul_i32 s4, s4, 22
	s_lshr_b32 s0, s2, 7
	s_add_i32 s0, s0, s4
	s_lshl_b32 s0, s0, 8
	s_and_b32 s5, s7, 0x7e
	s_or_b32 s0, s0, s6
	global_load_dwordx4 v[16:19], v[6:7], off nt
	s_or_b32 s98, s0, s5
	s_add_i32 s0, s33, s61
	s_add_i32 s0, s0, 3
	s_cmpk_gt_u32 s0, 0x15ff
	s_cselect_b32 s2, 0x7fffea00, 0
	s_cselect_b32 s4, s25, s15
	s_cselect_b32 s5, s24, s14
	s_cselect_b32 s6, 0x80, 0
	s_add_i32 s0, s0, s2
	s_lshl_b32 s7, s0, 1
	s_add_i32 s0, s7, 0x2c00
	s_lshl_b64 s[2:3], s[0:1], 12
	s_mul_hi_u32 s8, s0, 0xba2e8ba3
	s_add_u32 s2, s5, s2
	s_addc_u32 s3, s4, s3
	s_lshr_b32 s4, s8, 11
	v_lshl_add_u64 v[6:7], s[2:3], 0, v[0:1]
	s_mul_i32 s2, s4, 0x7ffff500
	s_add_i32 s2, s2, s0
	s_mul_i32 s4, s4, 22
	s_lshr_b32 s0, s2, 7
	s_add_i32 s0, s0, s4
	s_lshl_b32 s0, s0, 8
	s_and_b32 s5, s7, 0x7e
	s_or_b32 s0, s0, s6
	global_load_dwordx4 v[20:23], v[6:7], off nt
	s_or_b32 s99, s0, s5
	s_waitcnt vmcnt(0)
	s_mov_b32 s0, s96
	s_lshl_b64 s[2:3], s[0:1], 11
	v_lshl_add_u64 v[6:7], v[224:225], 0, s[2:3]
	v_cvt_pk_f16_f32 v11, v10, v11
	v_cvt_pk_f16_f32 v10, v8, v9
	global_store_dwordx2 v[6:7], v[10:11], off
	s_mov_b32 s0, s97
	s_lshl_b64 s[2:3], s[0:1], 11
	v_lshl_add_u64 v[6:7], v[224:225], 0, s[2:3]
	v_cvt_pk_f16_f32 v15, v14, v15
	v_cvt_pk_f16_f32 v14, v12, v13
	global_store_dwordx2 v[6:7], v[14:15], off
	s_mov_b32 s0, s98
	s_lshl_b64 s[2:3], s[0:1], 11
	v_lshl_add_u64 v[6:7], v[224:225], 0, s[2:3]
	v_cvt_pk_f16_f32 v19, v18, v19
	v_cvt_pk_f16_f32 v18, v16, v17
	global_store_dwordx2 v[6:7], v[18:19], off
	s_mov_b32 s0, s99
	s_lshl_b64 s[2:3], s[0:1], 11
	v_lshl_add_u64 v[6:7], v[224:225], 0, s[2:3]
	v_cvt_pk_f16_f32 v23, v22, v23
	v_cvt_pk_f16_f32 v22, v20, v21
	global_store_dwordx2 v[6:7], v[22:23], off
	s_add_i32 s61, s61, 4
	s_branch .Lg1a_fin4
.Lg1a_fin1:
	s_cmp_gt_i32 s61, 43
	s_cbranch_scc1 .LBB4_58
.LBB4_57:
	s_add_i32 s0, s33, s61
	s_cmpk_gt_u32 s0, 0x15ff
	s_cselect_b32 s2, 0x7fffea00, 0
	s_cselect_b32 s4, s25, s15
	s_cselect_b32 s5, s24, s14
	s_cselect_b32 s6, 0x80, 0
	s_add_i32 s0, s0, s2
	s_lshl_b32 s7, s0, 1
	s_add_i32 s0, s7, 0x2c00
	s_lshl_b64 s[2:3], s[0:1], 12
	s_mul_hi_u32 s8, s0, 0xba2e8ba3
	s_add_u32 s2, s5, s2
	s_addc_u32 s3, s4, s3
	s_lshr_b32 s4, s8, 11
	v_lshl_add_u64 v[6:7], s[2:3], 0, v[0:1]
	s_mul_i32 s2, s4, 0x7ffff500
	s_add_i32 s2, s2, s0
	s_mul_i32 s4, s4, 22
	s_lshr_b32 s0, s2, 7
	s_add_i32 s0, s0, s4
	s_lshl_b32 s0, s0, 8
	s_and_b32 s5, s7, 0x7e
	s_or_b32 s0, s0, s6
	global_load_dwordx4 v[2:5], v[6:7], off nt
	s_or_b32 s0, s0, s5
	s_add_i32 s7, s61, 1
	s_waitcnt vmcnt(0)
	s_lshl_b64 s[2:3], s[0:1], 11
	v_lshl_add_u64 v[6:7], v[224:225], 0, s[2:3]
	s_cmp_gt_i32 s61, 42
	s_mov_b32 s61, s7
	v_cvt_pk_f16_f32 v5, v4, v5
	v_cvt_pk_f16_f32 v4, v2, v3
	global_store_dwordx2 v[6:7], v[4:5], off
	s_cbranch_scc0 .LBB4_57

	.amdhsa_kernel _Z7k_gemm1ILi0EEvPKDF16_S1_PDF16_PK15HIP_vector_typeIiLj2EEPKfS8_S2_PKt
		.amdhsa_group_segment_fixed_size 0
		.amdhsa_private_segment_fixed_size 0
		.amdhsa_kernarg_size 64
		.amdhsa_user_sgpr_count 2
		.amdhsa_user_sgpr_dispatch_ptr 0
		.amdhsa_user_sgpr_queue_ptr 0
		.amdhsa_user_sgpr_kernarg_segment_ptr 1
		.amdhsa_user_sgpr_dispatch_id 0
		.amdhsa_user_sgpr_kernarg_preload_length 0
		.amdhsa_user_sgpr_kernarg_preload_offset 0
		.amdhsa_user_sgpr_private_segment_size 0
		.amdhsa_uses_dynamic_stack 0
		.amdhsa_enable_private_segment 0
		.amdhsa_system_sgpr_workgroup_id_x 1
		.amdhsa_system_sgpr_workgroup_id_y 0
		.amdhsa_system_sgpr_workgroup_id_z 0
		.amdhsa_system_sgpr_workgroup_info 0
		.amdhsa_system_vgpr_workitem_id 0
		.amdhsa_next_free_vgpr 256
		.amdhsa_next_free_sgpr 100
		.amdhsa_accum_offset 256
		.amdhsa_reserve_vcc 1
		.amdhsa_float_round_mode_32 0
		.amdhsa_float_round_mode_16_64 0
		.amdhsa_float_denorm_mode_32 3
		.amdhsa_float_denorm_mode_16_64 3
		.amdhsa_dx10_clamp 1
		.amdhsa_ieee_mode 1
		.amdhsa_fp16_overflow 0
		.amdhsa_tg_split 0
		.amdhsa_exception_fp_ieee_invalid_op 0
		.amdhsa_exception_fp_denorm_src 0
		.amdhsa_exception_fp_ieee_div_zero 0
		.amdhsa_exception_fp_ieee_overflow 0
		.amdhsa_exception_fp_ieee_underflow 0
		.amdhsa_exception_fp_ieee_inexact 0
		.amdhsa_exception_int_div_zero 0
	.end_amdhsa_kernel

.Lg1b_fin4:
	s_cmp_gt_i32 s63, 40
	s_cbranch_scc1 .Lg1b_fin1
	s_add_i32 s0, s33, s63
	s_lshl_b64 s[2:3], s[0:1], 13
	v_lshl_add_u64 v[4:5], v[224:225], 0, s[2:3]
	global_load_dwordx4 v[6:9], v[4:5], off nt
	s_add_u32 s2, s2, 0x2000
	s_addc_u32 s3, s3, 0
	v_lshl_add_u64 v[4:5], v[224:225], 0, s[2:3]
	global_load_dwordx4 v[10:13], v[4:5], off nt
	s_add_u32 s2, s2, 0x2000
	s_addc_u32 s3, s3, 0
	v_lshl_add_u64 v[4:5], v[224:225], 0, s[2:3]
	global_load_dwordx4 v[14:17], v[4:5], off nt
	s_add_u32 s2, s2, 0x2000
	s_addc_u32 s3, s3, 0
	v_lshl_add_u64 v[4:5], v[224:225], 0, s[2:3]
	global_load_dwordx4 v[18:21], v[4:5], off nt
	s_lshl_b64 s[2:3], s[0:1], 12
	s_waitcnt vmcnt(0)
	v_lshl_add_u64 v[4:5], v[220:221], 0, s[2:3]
	v_cvt_pk_f16_f32 v9, v8, v9
	v_cvt_pk_f16_f32 v8, v6, v7
	global_store_dwordx2 v[4:5], v[8:9], off
	s_add_u32 s2, s2, 0x1000
	s_addc_u32 s3, s3, 0
	v_lshl_add_u64 v[4:5], v[220:221], 0, s[2:3]
	v_cvt_pk_f16_f32 v13, v12, v13
	v_cvt_pk_f16_f32 v12, v10, v11
	global_store_dwordx2 v[4:5], v[12:13], off
	s_add_u32 s2, s2, 0x1000
	s_addc_u32 s3, s3, 0
	v_lshl_add_u64 v[4:5], v[220:221], 0, s[2:3]
	v_cvt_pk_f16_f32 v17, v16, v17
	v_cvt_pk_f16_f32 v16, v14, v15
	global_store_dwordx2 v[4:5], v[16:17], off
	s_add_u32 s2, s2, 0x1000
	s_addc_u32 s3, s3, 0
	v_lshl_add_u64 v[4:5], v[220:221], 0, s[2:3]
	v_cvt_pk_f16_f32 v21, v20, v21
	v_cvt_pk_f16_f32 v20, v18, v19
	global_store_dwordx2 v[4:5], v[20:21], off
	s_add_u32 s2, s2, 0x1000
	s_addc_u32 s3, s3, 0
	s_add_i32 s63, s63, 4
	s_branch .Lg1b_fin4
.Lg1b_fin1:
	s_cmp_gt_i32 s63, 43
	s_cbranch_scc1 .LBB5_58
.LBB5_57:
	s_add_i32 s0, s33, s63
	s_lshl_b64 s[2:3], s[0:1], 13
	v_lshl_add_u64 v[4:5], v[224:225], 0, s[2:3]
	global_load_dwordx4 v[0:3], v[4:5], off nt
	s_add_i32 s4, s63, 1
	s_lshl_b64 s[2:3], s[0:1], 12
	s_waitcnt vmcnt(0)
	v_lshl_add_u64 v[4:5], v[220:221], 0, s[2:3]
	s_cmp_gt_i32 s63, 42
	s_mov_b32 s63, s4
	v_cvt_pk_f16_f32 v3, v2, v3
	v_cvt_pk_f16_f32 v2, v0, v1
	global_store_dwordx2 v[4:5], v[2:3], off
	s_cbranch_scc0 .LBB5_57

amdhsa.kernels:
  - .agpr_count:     0
    .args:
      - .actual_access:  read_only
        .address_space:  global
        .offset:         0
        .size:           8
        .value_kind:     global_buffer
      - .actual_access:  read_only
        .address_space:  global
        .offset:         8
        .size:           8
        .value_kind:     global_buffer
      - .actual_access:  write_only
        .address_space:  global
        .offset:         16
        .size:           8
        .value_kind:     global_buffer
      - .actual_access:  write_only
        .address_space:  global
        .offset:         24
        .size:           8
        .value_kind:     global_buffer
      - .actual_access:  write_only
        .address_space:  global
        .offset:         32
        .size:           8
        .value_kind:     global_buffer
      - .actual_access:  write_only
        .address_space:  global
        .offset:         40
        .size:           8
        .value_kind:     global_buffer
    .group_segment_fixed_size: 256
    .kernarg_segment_align: 8
    .kernarg_segment_size: 48
    .language:       OpenCL C
    .language_version:
      - 2
      - 0
    .max_flat_workgroup_size: 256
    .name:           _Z10k_xscatterPKiS0_P15HIP_vector_typeIiLj2EEPtP4MetaS3_
    .private_segment_fixed_size: 0
    .sgpr_count:     41
    .sgpr_spill_count: 0
    .symbol:         _Z10k_xscatterPKiS0_P15HIP_vector_typeIiLj2EEPtP4MetaS3_.kd
    .uniform_work_group_size: 1
    .uses_dynamic_stack: false
    .vgpr_count:     55
    .vgpr_spill_count: 0
    .wavefront_size: 64
  - .agpr_count:     0
    .args:
      - .actual_access:  read_only
        .address_space:  global
        .offset:         0
        .size:           8
        .value_kind:     global_buffer
      - .actual_access:  read_only
        .address_space:  global
        .offset:         8
        .size:           8
        .value_kind:     global_buffer
      - .actual_access:  write_only
        .address_space:  global
        .offset:         16
        .size:           8
        .value_kind:     global_buffer
      - .actual_access:  write_only
        .address_space:  global
        .offset:         24
        .size:           8
        .value_kind:     global_buffer
      - .actual_access:  write_only
        .address_space:  global
        .offset:         32
        .size:           8
        .value_kind:     global_buffer
      - .actual_access:  read_only
        .address_space:  global
        .offset:         40
        .size:           8
        .value_kind:     global_buffer
      - .actual_access:  read_only
        .address_space:  global
        .offset:         48
        .size:           8
        .value_kind:     global_buffer
      - .actual_access:  write_only
        .address_space:  global
        .offset:         56
        .size:           8
        .value_kind:     global_buffer
      - .actual_access:  write_only
        .address_space:  global
        .offset:         64
        .size:           8
        .value_kind:     global_buffer
    .group_segment_fixed_size: 4096
    .kernarg_segment_align: 8
    .kernarg_segment_size: 72
    .language:       OpenCL C
    .language_version:
      - 2
      - 0
    .max_flat_workgroup_size: 256
    .name:           _Z5k_prePKfS0_PiP15HIP_vector_typeIfLj2EES1_S0_S0_PDF16_S5_
    .private_segment_fixed_size: 0
    .sgpr_count:     38
    .sgpr_spill_count: 0
    .symbol:         _Z5k_prePKfS0_PiP15HIP_vector_typeIfLj2EES1_S0_S0_PDF16_S5_.kd
    .uniform_work_group_size: 1
    .uses_dynamic_stack: false
    .vgpr_count:     128
    .vgpr_spill_count: 0
    .wavefront_size: 64
  - .agpr_count:     0
    .args:
      - .address_space:  global
        .offset:         0
        .size:           8
        .value_kind:     global_buffer
      - .address_space:  global
        .offset:         8
        .size:           8
        .value_kind:     global_buffer
      - .actual_access:  write_only
        .address_space:  global
        .offset:         16
        .size:           8
        .value_kind:     global_buffer
      - .actual_access:  read_only
        .address_space:  global
        .offset:         24
        .size:           8
        .value_kind:     global_buffer
    .group_segment_fixed_size: 0
    .kernarg_segment_align: 8
    .kernarg_segment_size: 32
    .language:       OpenCL C
    .language_version:
      - 2
      - 0
    .max_flat_workgroup_size: 512
    .name:           _Z7k_gemm2PKDF16_S0_PDF16_PK15HIP_vector_typeIiLj2EE
    .private_segment_fixed_size: 0
    .sgpr_count:     74
    .sgpr_spill_count: 0
    .symbol:         _Z7k_gemm2PKDF16_S0_PDF16_PK15HIP_vector_typeIiLj2EE.kd
    .uniform_work_group_size: 1
    .uses_dynamic_stack: false
    .vgpr_count:     226
    .vgpr_spill_count: 0
    .wavefront_size: 64
  - .agpr_count:     0
    .args:
      - .actual_access:  read_only
        .address_space:  global
        .offset:         0
        .size:           8
        .value_kind:     global_buffer
      - .actual_access:  read_only
        .address_space:  global
        .offset:         8
        .size:           8
        .value_kind:     global_buffer
      - .actual_access:  read_only
        .address_space:  global
        .offset:         16
        .size:           8
        .value_kind:     global_buffer
      - .actual_access:  write_only
        .address_space:  global
        .offset:         24
        .size:           8
        .value_kind:     global_buffer
    .group_segment_fixed_size: 0
    .kernarg_segment_align: 8
    .kernarg_segment_size: 32
    .language:       OpenCL C
    .language_version:
      - 2
      - 0
    .max_flat_workgroup_size: 256
    .name:           _Z9k_combinePKDF16_PK15HIP_vector_typeIiLj2EEPKS1_IfLj2EEPf
    .private_segment_fixed_size: 0
    .sgpr_count:     30
    .sgpr_spill_count: 0
    .symbol:         _Z9k_combinePKDF16_PK15HIP_vector_typeIiLj2EEPKS1_IfLj2EEPf.kd
    .uniform_work_group_size: 1
    .uses_dynamic_stack: false
    .vgpr_count:     64
    .vgpr_spill_count: 0
    .wavefront_size: 64
  - .agpr_count:     0
    .args:
      - .address_space:  global
        .offset:         0
        .size:           8
        .value_kind:     global_buffer
      - .address_space:  global
        .offset:         8
        .size:           8
        .value_kind:     global_buffer
      - .actual_access:  write_only
        .address_space:  global
        .offset:         16
        .size:           8
        .value_kind:     global_buffer
      - .actual_access:  read_only
        .address_space:  global
        .offset:         24
        .size:           8
        .value_kind:     global_buffer
      - .address_space:  global
        .offset:         32
        .size:           8
        .value_kind:     global_buffer
      - .address_space:  global
        .offset:         40
        .size:           8
        .value_kind:     global_buffer
      - .actual_access:  write_only
        .address_space:  global
        .offset:         48
        .size:           8
        .value_kind:     global_buffer
      - .address_space:  global
        .offset:         56
        .size:           8
        .value_kind:     global_buffer
    .group_segment_fixed_size: 0
    .kernarg_segment_align: 8
    .kernarg_segment_size: 64
    .language:       OpenCL C
    .language_version:
      - 2
      - 0
    .max_flat_workgroup_size: 512
    .name:           _Z7k_gemm1ILi0EEvPKDF16_S1_PDF16_PK15HIP_vector_typeIiLj2EEPKfS8_S2_PKt
    .private_segment_fixed_size: 0
    .sgpr_count:     106
    .sgpr_spill_count: 0
    .symbol:         _Z7k_gemm1ILi0EEvPKDF16_S1_PDF16_PK15HIP_vector_typeIiLj2EEPKfS8_S2_PKt.kd
    .uniform_work_group_size: 1
    .uses_dynamic_stack: false
    .vgpr_count:     256
    .vgpr_spill_count: 0
    .wavefront_size: 64
  - .agpr_count:     0
    .args:
      - .address_space:  global
        .offset:         0
        .size:           8
        .value_kind:     global_buffer
      - .address_space:  global
        .offset:         8
        .size:           8
        .value_kind:     global_buffer
      - .actual_access:  write_only
        .address_space:  global
        .offset:         16
        .size:           8
        .value_kind:     global_buffer
      - .actual_access:  read_only
        .address_space:  global
        .offset:         24
        .size:           8
        .value_kind:     global_buffer
      - .address_space:  global
        .offset:         32
        .size:           8
        .value_kind:     global_buffer
      - .actual_access:  read_only
        .address_space:  global
        .offset:         40
        .size:           8
        .value_kind:     global_buffer
      - .actual_access:  write_only
        .address_space:  global
        .offset:         48
        .size:           8
        .value_kind:     global_buffer
      - .address_space:  global
        .offset:         56
        .size:           8
        .value_kind:     global_buffer
    .group_segment_fixed_size: 0
    .kernarg_segment_align: 8
    .kernarg_segment_size: 64
    .language:       OpenCL C
    .language_version:
      - 2
      - 0
    .max_flat_workgroup_size: 512
    .name:           _Z7k_gemm1ILi1EEvPKDF16_S1_PDF16_PK15HIP_vector_typeIiLj2EEPKfS8_S2_PKt
    .private_segment_fixed_size: 0
    .sgpr_count:     96
    .sgpr_spill_count: 0
    .symbol:         _Z7k_gemm1ILi1EEvPKDF16_S1_PDF16_PK15HIP_vector_typeIiLj2EEPKfS8_S2_PKt.kd
    .uniform_work_group_size: 1
    .uses_dynamic_stack: false
    .vgpr_count:     254
    .vgpr_spill_count: 0
    .wavefront_size: 64
